# attention-A: V fragment reads issued before the K-next reads, so the wait in front of the first P.V MFMA is a counted lgkmcnt(8) (K-next data is only needed after the next tile barrier); on top of v70
# speedup vs baseline: 1.0069x; 1.0069x over previous
.LBB0_419:
	v_mfma_scale_f32_32x32x64_f8f6f4 v[112:127], v[228:233], v[182:187], v[80:95], v217, v216 op_sel_hi:[0,0,0] cbsz:2 blgp:2
	v_exp_f32_e32 v128, v128
	v_exp_f32_e32 v129, v129
	v_exp_f32_e32 v130, v130
	v_exp_f32_e32 v131, v131
	v_mfma_scale_f32_32x32x64_f8f6f4 v[96:111], v[234:239], v[182:187], v[80:95], v217, v216 op_sel_hi:[0,0,0] cbsz:2 blgp:2
	v_exp_f32_e32 v132, v132
	v_exp_f32_e32 v133, v133
	v_exp_f32_e32 v134, v134
	v_exp_f32_e32 v135, v135
	v_mfma_scale_f32_32x32x64_f8f6f4 v[112:127], v[240:245], v[176:181], v[112:127], v217, v216 op_sel_hi:[0,0,0] cbsz:2 blgp:2
	v_exp_f32_e32 v136, v136
	v_exp_f32_e32 v137, v137
	v_exp_f32_e32 v138, v138
	v_exp_f32_e32 v139, v139
	v_mfma_scale_f32_32x32x64_f8f6f4 v[96:111], v[246:251], v[176:181], v[96:111], v217, v216 op_sel_hi:[0,0,0] cbsz:2 blgp:2
	ds_read_b128 v[206:209], v163 offset:24576
	ds_read_b64 v[210:211], v220 offset:24576
	ds_read_b128 v[200:203], v163 offset:26624
	ds_read_b64 v[204:205], v220 offset:26624
	ds_read_b128 v[194:197], v163 offset:28672
	ds_read_b64 v[198:199], v220 offset:28672
	ds_read_b128 v[188:191], v163 offset:30720
	ds_read_b64 v[192:193], v220 offset:30720
	ds_read_b128 v[228:231], v223
	ds_read_b64 v[232:233], v224
	ds_read_b128 v[234:237], v223 offset:4096
	ds_read_b64 v[238:239], v224 offset:4096
	ds_read_b128 v[240:243], v221
	ds_read_b64 v[244:245], v222
	ds_read_b128 v[246:249], v221 offset:4096
	ds_read_b64 v[250:251], v222 offset:4096
	v_exp_f32_e32 v140, v140
	v_exp_f32_e32 v141, v141
	v_exp_f32_e32 v142, v142
	v_exp_f32_e32 v143, v143
	v_max_f32_e32 v225, v112, v113
	v_cvt_scalef32_2xpk16_bf6_f32 v[128:133], v[144:159], v[128:143], 1.0
	v_max3_f32 v225, v225, v114, v115
	v_max3_f32 v225, v225, v116, v117
	v_mfma_scale_f32_32x32x64_f8f6f4 v[64:79], v[128:133], v[168:173], v[64:79], v218, v218 op_sel_hi:[0,0,0] cbsz:3 blgp:2
	s_waitcnt lgkmcnt(8)
	v_mfma_scale_f32_32x32x64_f8f6f4 v[0:15], v[128:133], v[206:211], v[0:15], v218, v217 op_sel_hi:[0,0,0] cbsz:3 blgp:2
	v_max3_f32 v225, v225, v118, v119
	v_max3_f32 v225, v225, v120, v121
	v_max3_f32 v225, v225, v122, v123
	v_mfma_scale_f32_32x32x64_f8f6f4 v[48:63], v[128:133], v[200:205], v[48:63], v218, v217 op_sel_hi:[0,0,0] cbsz:3 blgp:2
	v_max3_f32 v225, v225, v124, v125
	v_max3_f32 v225, v225, v126, v127
	v_max3_f32 v225, v225, v96, v97
	v_max3_f32 v225, v225, v98, v99
	v_mfma_scale_f32_32x32x64_f8f6f4 v[32:47], v[128:133], v[194:199], v[32:47], v218, v217 op_sel_hi:[0,0,0] cbsz:3 blgp:2
	v_max3_f32 v225, v225, v100, v101
	v_max3_f32 v225, v225, v102, v103
	v_max3_f32 v225, v225, v104, v105
	v_max3_f32 v225, v225, v106, v107
	v_mfma_scale_f32_32x32x64_f8f6f4 v[16:31], v[128:133], v[188:193], v[16:31], v218, v217 op_sel_hi:[0,0,0] cbsz:3 blgp:2
	v_max3_f32 v225, v225, v108, v109
	v_max3_f32 v225, v225, v110, v111
	v_cmp_nge_f32_e32 vcc, s2, v225
	s_cbranch_vccnz .LBB0_444

.LBB0_437:
	v_mfma_scale_f32_32x32x64_f8f6f4 v[144:159], v[228:233], v[182:187], v[80:95], v217, v216 op_sel_hi:[0,0,0] cbsz:2 blgp:2
	v_exp_f32_e32 v96, v96
	v_exp_f32_e32 v97, v97
	v_exp_f32_e32 v98, v98
	v_exp_f32_e32 v99, v99
	v_mfma_scale_f32_32x32x64_f8f6f4 v[128:143], v[234:239], v[182:187], v[80:95], v217, v216 op_sel_hi:[0,0,0] cbsz:2 blgp:2
	v_exp_f32_e32 v100, v100
	v_exp_f32_e32 v101, v101
	v_exp_f32_e32 v102, v102
	v_exp_f32_e32 v103, v103
	v_mfma_scale_f32_32x32x64_f8f6f4 v[144:159], v[240:245], v[176:181], v[144:159], v217, v216 op_sel_hi:[0,0,0] cbsz:2 blgp:2
	v_exp_f32_e32 v104, v104
	v_exp_f32_e32 v105, v105
	v_exp_f32_e32 v106, v106
	v_exp_f32_e32 v107, v107
	v_mfma_scale_f32_32x32x64_f8f6f4 v[128:143], v[246:251], v[176:181], v[128:143], v217, v216 op_sel_hi:[0,0,0] cbsz:2 blgp:2
	ds_read_b128 v[206:209], v163 offset:32768
	ds_read_b64 v[210:211], v220 offset:32768
	ds_read_b128 v[200:203], v163 offset:34816
	ds_read_b64 v[204:205], v220 offset:34816
	ds_read_b128 v[194:197], v163 offset:36864
	ds_read_b64 v[198:199], v220 offset:36864
	ds_read_b128 v[188:191], v163 offset:38912
	ds_read_b64 v[192:193], v220 offset:38912
	ds_read_b128 v[228:231], v223 offset:8192
	ds_read_b64 v[232:233], v224 offset:8192
	ds_read_b128 v[234:237], v223 offset:12288
	ds_read_b64 v[238:239], v224 offset:12288
	ds_read_b128 v[240:243], v221 offset:8192
	ds_read_b64 v[244:245], v222 offset:8192
	ds_read_b128 v[246:249], v221 offset:12288
	ds_read_b64 v[250:251], v222 offset:12288
	v_exp_f32_e32 v108, v108
	v_exp_f32_e32 v109, v109
	v_exp_f32_e32 v110, v110
	v_exp_f32_e32 v111, v111
	v_max_f32_e32 v212, v144, v145
	v_cvt_scalef32_2xpk16_bf6_f32 v[96:101], v[112:127], v[96:111], 1.0
	v_max3_f32 v212, v212, v146, v147
	v_max3_f32 v212, v212, v148, v149
	v_mfma_scale_f32_32x32x64_f8f6f4 v[64:79], v[96:101], v[168:173], v[64:79], v218, v218 op_sel_hi:[0,0,0] cbsz:3 blgp:2
	s_waitcnt lgkmcnt(8)
	v_mfma_scale_f32_32x32x64_f8f6f4 v[0:15], v[96:101], v[206:211], v[0:15], v218, v217 op_sel_hi:[0,0,0] cbsz:3 blgp:2
	v_max3_f32 v212, v212, v150, v151
	v_max3_f32 v212, v212, v152, v153
	v_max3_f32 v212, v212, v154, v155
	v_mfma_scale_f32_32x32x64_f8f6f4 v[48:63], v[96:101], v[200:205], v[48:63], v218, v217 op_sel_hi:[0,0,0] cbsz:3 blgp:2
	v_max3_f32 v212, v212, v156, v157
	v_max3_f32 v212, v212, v158, v159
	v_max3_f32 v212, v212, v128, v129
	v_max3_f32 v212, v212, v130, v131
	v_mfma_scale_f32_32x32x64_f8f6f4 v[32:47], v[96:101], v[194:199], v[32:47], v218, v217 op_sel_hi:[0,0,0] cbsz:3 blgp:2
	v_max3_f32 v212, v212, v132, v133
	v_max3_f32 v212, v212, v134, v135
	v_max3_f32 v212, v212, v136, v137
	v_max3_f32 v212, v212, v138, v139
	v_mfma_scale_f32_32x32x64_f8f6f4 v[16:31], v[96:101], v[188:193], v[16:31], v218, v217 op_sel_hi:[0,0,0] cbsz:3 blgp:2
	v_max3_f32 v212, v212, v140, v141
	v_max3_f32 v212, v212, v142, v143
	v_cmp_nge_f32_e32 vcc, s2, v212
	s_cbranch_vccnz .LBB0_445
